# unrolls two 16-trip staging loops (silu(c) for adaLN, router weights to LDS): all loads issued before the waits
# speedup vs baseline: 1.0191x; 1.0029x over previous
.LBB0_5:
	s_or_b64 exec, exec, s[4:5]
	s_and_b32 s66, s72, 0xffffffc0
	s_cmp_lt_i32 s86, 1
	s_cselect_b64 s[4:5], -1, 0
	s_cmp_gt_i32 s87, 0
	s_cselect_b64 s[6:7], -1, 0
	s_and_b64 s[12:13], s[4:5], s[6:7]
	s_andn2_b64 vcc, exec, s[12:13]
	v_writelane_b32 v253, s66, 2
	s_cbranch_vccnz .LBB0_186
	s_mov_b64 s[14:15], s[70:71]
	v_mbcnt_lo_u32_b32 v35, -1, 0
	v_mbcnt_hi_u32_b32 v35, -1, v35
	s_load_dwordx2 s[16:17], s[14:15], 0x100
	v_add_u32_e32 v0, s66, v35
	v_and_b32_e32 v34, 63, v35
	v_readfirstlane_b32 s4, v0
	s_ashr_i32 s36, s4, 6
	s_cmpk_gt_i32 s2, 0xbf
	s_waitcnt lgkmcnt(0)
	s_barrier
	s_cbranch_scc1 .LBB0_15
	s_movk_i32 s4, 0x2000
	v_cmp_gt_i32_e32 vcc, s4, v0
	s_and_saveexec_b64 s[4:5], vcc
	s_cbranch_execz .LBB0_10
	s_load_dwordx2 s[6:7], s[14:15], 0x8
	s_lshl_b32 s8, s72, 2
	s_and_b32 s8, s8, 0xffffff00
	s_add_i32 s8, s8, 0
	v_ashrrev_i32_e32 v1, 31, v0
	v_add_u32_e32 v4, 0xfffffe00, v0
	v_lshl_add_u32 v5, v35, 2, s8
	s_waitcnt lgkmcnt(0)
	v_lshl_add_u64 v[2:3], v[0:1], 2, s[6:7]
	s_mov_b64 s[6:7], 0
	s_mov_b64 s[8:9], 0x800
	s_movk_i32 s10, 0x1dff
	global_load_dword v12, v[2:3], off
	v_lshl_add_u64 v[2:3], v[2:3], 0, s[8:9]
	global_load_dword v13, v[2:3], off
	v_lshl_add_u64 v[2:3], v[2:3], 0, s[8:9]
	global_load_dword v14, v[2:3], off
	v_lshl_add_u64 v[2:3], v[2:3], 0, s[8:9]
	global_load_dword v15, v[2:3], off
	v_lshl_add_u64 v[2:3], v[2:3], 0, s[8:9]
	global_load_dword v16, v[2:3], off
	v_lshl_add_u64 v[2:3], v[2:3], 0, s[8:9]
	global_load_dword v17, v[2:3], off
	v_lshl_add_u64 v[2:3], v[2:3], 0, s[8:9]
	global_load_dword v18, v[2:3], off
	v_lshl_add_u64 v[2:3], v[2:3], 0, s[8:9]
	global_load_dword v19, v[2:3], off
	v_lshl_add_u64 v[2:3], v[2:3], 0, s[8:9]
	global_load_dword v20, v[2:3], off
	v_lshl_add_u64 v[2:3], v[2:3], 0, s[8:9]
	global_load_dword v21, v[2:3], off
	v_lshl_add_u64 v[2:3], v[2:3], 0, s[8:9]
	global_load_dword v22, v[2:3], off
	v_lshl_add_u64 v[2:3], v[2:3], 0, s[8:9]
	global_load_dword v23, v[2:3], off
	v_lshl_add_u64 v[2:3], v[2:3], 0, s[8:9]
	global_load_dword v24, v[2:3], off
	v_lshl_add_u64 v[2:3], v[2:3], 0, s[8:9]
	global_load_dword v25, v[2:3], off
	v_lshl_add_u64 v[2:3], v[2:3], 0, s[8:9]
	global_load_dword v26, v[2:3], off
	v_lshl_add_u64 v[2:3], v[2:3], 0, s[8:9]
	global_load_dword v27, v[2:3], off
	v_lshl_add_u64 v[2:3], v[2:3], 0, s[8:9]
	s_waitcnt vmcnt(15)
	v_mul_f32_e32 v6, 0xbfb8aa3b, v12
	v_exp_f32_e32 v6, v6
	s_nop 0
	v_add_f32_e32 v6, 1.0, v6
	v_div_scale_f32 v7, s[18:19], v6, v6, v12
	v_rcp_f32_e32 v8, v7
	v_div_scale_f32 v9, vcc, v12, v6, v12
	v_fma_f32 v10, -v7, v8, 1.0
	v_fmac_f32_e32 v8, v10, v8
	v_mul_f32_e32 v10, v9, v8
	v_fma_f32 v11, -v7, v10, v9
	v_fmac_f32_e32 v10, v11, v8
	v_fma_f32 v7, -v7, v10, v9
	v_div_fmas_f32 v7, v7, v8, v10
	v_div_fixup_f32 v12, v7, v6, v12
	ds_write_b32 v5, v12
	v_add_u32_e32 v5, 0x800, v5
	s_waitcnt vmcnt(14)
	v_mul_f32_e32 v6, 0xbfb8aa3b, v13
	v_exp_f32_e32 v6, v6
	s_nop 0
	v_add_f32_e32 v6, 1.0, v6
	v_div_scale_f32 v7, s[18:19], v6, v6, v13
	v_rcp_f32_e32 v8, v7
	v_div_scale_f32 v9, vcc, v13, v6, v13
	v_fma_f32 v10, -v7, v8, 1.0
	v_fmac_f32_e32 v8, v10, v8
	v_mul_f32_e32 v10, v9, v8
	v_fma_f32 v11, -v7, v10, v9
	v_fmac_f32_e32 v10, v11, v8
	v_fma_f32 v7, -v7, v10, v9
	v_div_fmas_f32 v7, v7, v8, v10
	v_div_fixup_f32 v13, v7, v6, v13
	ds_write_b32 v5, v13
	v_add_u32_e32 v5, 0x800, v5
	s_waitcnt vmcnt(13)
	v_mul_f32_e32 v6, 0xbfb8aa3b, v14
	v_exp_f32_e32 v6, v6
	s_nop 0
	v_add_f32_e32 v6, 1.0, v6
	v_div_scale_f32 v7, s[18:19], v6, v6, v14
	v_rcp_f32_e32 v8, v7
	v_div_scale_f32 v9, vcc, v14, v6, v14
	v_fma_f32 v10, -v7, v8, 1.0
	v_fmac_f32_e32 v8, v10, v8
	v_mul_f32_e32 v10, v9, v8
	v_fma_f32 v11, -v7, v10, v9
	v_fmac_f32_e32 v10, v11, v8
	v_fma_f32 v7, -v7, v10, v9
	v_div_fmas_f32 v7, v7, v8, v10
	v_div_fixup_f32 v14, v7, v6, v14
	ds_write_b32 v5, v14
	v_add_u32_e32 v5, 0x800, v5
	s_waitcnt vmcnt(12)
	v_mul_f32_e32 v6, 0xbfb8aa3b, v15
	v_exp_f32_e32 v6, v6
	s_nop 0
	v_add_f32_e32 v6, 1.0, v6
	v_div_scale_f32 v7, s[18:19], v6, v6, v15
	v_rcp_f32_e32 v8, v7
	v_div_scale_f32 v9, vcc, v15, v6, v15
	v_fma_f32 v10, -v7, v8, 1.0
	v_fmac_f32_e32 v8, v10, v8
	v_mul_f32_e32 v10, v9, v8
	v_fma_f32 v11, -v7, v10, v9
	v_fmac_f32_e32 v10, v11, v8
	v_fma_f32 v7, -v7, v10, v9
	v_div_fmas_f32 v7, v7, v8, v10
	v_div_fixup_f32 v15, v7, v6, v15
	ds_write_b32 v5, v15
	v_add_u32_e32 v5, 0x800, v5
	s_waitcnt vmcnt(11)
	v_mul_f32_e32 v6, 0xbfb8aa3b, v16
	v_exp_f32_e32 v6, v6
	s_nop 0
	v_add_f32_e32 v6, 1.0, v6
	v_div_scale_f32 v7, s[18:19], v6, v6, v16
	v_rcp_f32_e32 v8, v7
	v_div_scale_f32 v9, vcc, v16, v6, v16
	v_fma_f32 v10, -v7, v8, 1.0
	v_fmac_f32_e32 v8, v10, v8
	v_mul_f32_e32 v10, v9, v8
	v_fma_f32 v11, -v7, v10, v9
	v_fmac_f32_e32 v10, v11, v8
	v_fma_f32 v7, -v7, v10, v9
	v_div_fmas_f32 v7, v7, v8, v10
	v_div_fixup_f32 v16, v7, v6, v16
	ds_write_b32 v5, v16
	v_add_u32_e32 v5, 0x800, v5
	s_waitcnt vmcnt(10)
	v_mul_f32_e32 v6, 0xbfb8aa3b, v17
	v_exp_f32_e32 v6, v6
	s_nop 0
	v_add_f32_e32 v6, 1.0, v6
	v_div_scale_f32 v7, s[18:19], v6, v6, v17
	v_rcp_f32_e32 v8, v7
	v_div_scale_f32 v9, vcc, v17, v6, v17
	v_fma_f32 v10, -v7, v8, 1.0
	v_fmac_f32_e32 v8, v10, v8
	v_mul_f32_e32 v10, v9, v8
	v_fma_f32 v11, -v7, v10, v9
	v_fmac_f32_e32 v10, v11, v8
	v_fma_f32 v7, -v7, v10, v9
	v_div_fmas_f32 v7, v7, v8, v10
	v_div_fixup_f32 v17, v7, v6, v17
	ds_write_b32 v5, v17
	v_add_u32_e32 v5, 0x800, v5
	s_waitcnt vmcnt(9)
	v_mul_f32_e32 v6, 0xbfb8aa3b, v18
	v_exp_f32_e32 v6, v6
	s_nop 0
	v_add_f32_e32 v6, 1.0, v6
	v_div_scale_f32 v7, s[18:19], v6, v6, v18
	v_rcp_f32_e32 v8, v7
	v_div_scale_f32 v9, vcc, v18, v6, v18
	v_fma_f32 v10, -v7, v8, 1.0
	v_fmac_f32_e32 v8, v10, v8
	v_mul_f32_e32 v10, v9, v8
	v_fma_f32 v11, -v7, v10, v9
	v_fmac_f32_e32 v10, v11, v8
	v_fma_f32 v7, -v7, v10, v9
	v_div_fmas_f32 v7, v7, v8, v10
	v_div_fixup_f32 v18, v7, v6, v18
	ds_write_b32 v5, v18
	v_add_u32_e32 v5, 0x800, v5
	s_waitcnt vmcnt(8)
	v_mul_f32_e32 v6, 0xbfb8aa3b, v19
	v_exp_f32_e32 v6, v6
	s_nop 0
	v_add_f32_e32 v6, 1.0, v6
	v_div_scale_f32 v7, s[18:19], v6, v6, v19
	v_rcp_f32_e32 v8, v7
	v_div_scale_f32 v9, vcc, v19, v6, v19
	v_fma_f32 v10, -v7, v8, 1.0
	v_fmac_f32_e32 v8, v10, v8
	v_mul_f32_e32 v10, v9, v8
	v_fma_f32 v11, -v7, v10, v9
	v_fmac_f32_e32 v10, v11, v8
	v_fma_f32 v7, -v7, v10, v9
	v_div_fmas_f32 v7, v7, v8, v10
	v_div_fixup_f32 v19, v7, v6, v19
	ds_write_b32 v5, v19
	v_add_u32_e32 v5, 0x800, v5
	s_waitcnt vmcnt(7)
	v_mul_f32_e32 v6, 0xbfb8aa3b, v20
	v_exp_f32_e32 v6, v6
	s_nop 0
	v_add_f32_e32 v6, 1.0, v6
	v_div_scale_f32 v7, s[18:19], v6, v6, v20
	v_rcp_f32_e32 v8, v7
	v_div_scale_f32 v9, vcc, v20, v6, v20
	v_fma_f32 v10, -v7, v8, 1.0
	v_fmac_f32_e32 v8, v10, v8
	v_mul_f32_e32 v10, v9, v8
	v_fma_f32 v11, -v7, v10, v9
	v_fmac_f32_e32 v10, v11, v8
	v_fma_f32 v7, -v7, v10, v9
	v_div_fmas_f32 v7, v7, v8, v10
	v_div_fixup_f32 v20, v7, v6, v20
	ds_write_b32 v5, v20
	v_add_u32_e32 v5, 0x800, v5
	s_waitcnt vmcnt(6)
	v_mul_f32_e32 v6, 0xbfb8aa3b, v21
	v_exp_f32_e32 v6, v6
	s_nop 0
	v_add_f32_e32 v6, 1.0, v6
	v_div_scale_f32 v7, s[18:19], v6, v6, v21
	v_rcp_f32_e32 v8, v7
	v_div_scale_f32 v9, vcc, v21, v6, v21
	v_fma_f32 v10, -v7, v8, 1.0
	v_fmac_f32_e32 v8, v10, v8
	v_mul_f32_e32 v10, v9, v8
	v_fma_f32 v11, -v7, v10, v9
	v_fmac_f32_e32 v10, v11, v8
	v_fma_f32 v7, -v7, v10, v9
	v_div_fmas_f32 v7, v7, v8, v10
	v_div_fixup_f32 v21, v7, v6, v21
	ds_write_b32 v5, v21
	v_add_u32_e32 v5, 0x800, v5
	s_waitcnt vmcnt(5)
	v_mul_f32_e32 v6, 0xbfb8aa3b, v22
	v_exp_f32_e32 v6, v6
	s_nop 0
	v_add_f32_e32 v6, 1.0, v6
	v_div_scale_f32 v7, s[18:19], v6, v6, v22
	v_rcp_f32_e32 v8, v7
	v_div_scale_f32 v9, vcc, v22, v6, v22
	v_fma_f32 v10, -v7, v8, 1.0
	v_fmac_f32_e32 v8, v10, v8
	v_mul_f32_e32 v10, v9, v8
	v_fma_f32 v11, -v7, v10, v9
	v_fmac_f32_e32 v10, v11, v8
	v_fma_f32 v7, -v7, v10, v9
	v_div_fmas_f32 v7, v7, v8, v10
	v_div_fixup_f32 v22, v7, v6, v22
	ds_write_b32 v5, v22
	v_add_u32_e32 v5, 0x800, v5
	s_waitcnt vmcnt(4)
	v_mul_f32_e32 v6, 0xbfb8aa3b, v23
	v_exp_f32_e32 v6, v6
	s_nop 0
	v_add_f32_e32 v6, 1.0, v6
	v_div_scale_f32 v7, s[18:19], v6, v6, v23
	v_rcp_f32_e32 v8, v7
	v_div_scale_f32 v9, vcc, v23, v6, v23
	v_fma_f32 v10, -v7, v8, 1.0
	v_fmac_f32_e32 v8, v10, v8
	v_mul_f32_e32 v10, v9, v8
	v_fma_f32 v11, -v7, v10, v9
	v_fmac_f32_e32 v10, v11, v8
	v_fma_f32 v7, -v7, v10, v9
	v_div_fmas_f32 v7, v7, v8, v10
	v_div_fixup_f32 v23, v7, v6, v23
	ds_write_b32 v5, v23
	v_add_u32_e32 v5, 0x800, v5
	s_waitcnt vmcnt(3)
	v_mul_f32_e32 v6, 0xbfb8aa3b, v24
	v_exp_f32_e32 v6, v6
	s_nop 0
	v_add_f32_e32 v6, 1.0, v6
	v_div_scale_f32 v7, s[18:19], v6, v6, v24
	v_rcp_f32_e32 v8, v7
	v_div_scale_f32 v9, vcc, v24, v6, v24
	v_fma_f32 v10, -v7, v8, 1.0
	v_fmac_f32_e32 v8, v10, v8
	v_mul_f32_e32 v10, v9, v8
	v_fma_f32 v11, -v7, v10, v9
	v_fmac_f32_e32 v10, v11, v8
	v_fma_f32 v7, -v7, v10, v9
	v_div_fmas_f32 v7, v7, v8, v10
	v_div_fixup_f32 v24, v7, v6, v24
	ds_write_b32 v5, v24
	v_add_u32_e32 v5, 0x800, v5
	s_waitcnt vmcnt(2)
	v_mul_f32_e32 v6, 0xbfb8aa3b, v25
	v_exp_f32_e32 v6, v6
	s_nop 0
	v_add_f32_e32 v6, 1.0, v6
	v_div_scale_f32 v7, s[18:19], v6, v6, v25
	v_rcp_f32_e32 v8, v7
	v_div_scale_f32 v9, vcc, v25, v6, v25
	v_fma_f32 v10, -v7, v8, 1.0
	v_fmac_f32_e32 v8, v10, v8
	v_mul_f32_e32 v10, v9, v8
	v_fma_f32 v11, -v7, v10, v9
	v_fmac_f32_e32 v10, v11, v8
	v_fma_f32 v7, -v7, v10, v9
	v_div_fmas_f32 v7, v7, v8, v10
	v_div_fixup_f32 v25, v7, v6, v25
	ds_write_b32 v5, v25
	v_add_u32_e32 v5, 0x800, v5
	s_waitcnt vmcnt(1)
	v_mul_f32_e32 v6, 0xbfb8aa3b, v26
	v_exp_f32_e32 v6, v6
	s_nop 0
	v_add_f32_e32 v6, 1.0, v6
	v_div_scale_f32 v7, s[18:19], v6, v6, v26
	v_rcp_f32_e32 v8, v7
	v_div_scale_f32 v9, vcc, v26, v6, v26
	v_fma_f32 v10, -v7, v8, 1.0
	v_fmac_f32_e32 v8, v10, v8
	v_mul_f32_e32 v10, v9, v8
	v_fma_f32 v11, -v7, v10, v9
	v_fmac_f32_e32 v10, v11, v8
	v_fma_f32 v7, -v7, v10, v9
	v_div_fmas_f32 v7, v7, v8, v10
	v_div_fixup_f32 v26, v7, v6, v26
	ds_write_b32 v5, v26
	v_add_u32_e32 v5, 0x800, v5
	s_waitcnt vmcnt(0)
	v_mul_f32_e32 v6, 0xbfb8aa3b, v27
	v_exp_f32_e32 v6, v6
	s_nop 0
	v_add_f32_e32 v6, 1.0, v6
	v_div_scale_f32 v7, s[18:19], v6, v6, v27
	v_rcp_f32_e32 v8, v7
	v_div_scale_f32 v9, vcc, v27, v6, v27
	v_fma_f32 v10, -v7, v8, 1.0
	v_fmac_f32_e32 v8, v10, v8
	v_mul_f32_e32 v10, v9, v8
	v_fma_f32 v11, -v7, v10, v9
	v_fmac_f32_e32 v10, v11, v8
	v_fma_f32 v7, -v7, v10, v9
	v_div_fmas_f32 v7, v7, v8, v10
	v_div_fixup_f32 v27, v7, v6, v27
	ds_write_b32 v5, v27
	v_add_u32_e32 v5, 0x800, v5

.LBB0_1288:
	s_andn2_b64 vcc, exec, s[4:5]
	s_cbranch_vccnz .LBB0_1432
	s_mov_b64 s[56:57], s[70:71]
	v_mbcnt_lo_u32_b32 v0, -1, 0
	v_mbcnt_hi_u32_b32 v0, -1, v0
	s_load_dwordx2 s[58:59], s[56:57], 0x100
	v_add_u32_e32 v22, s67, v0
	s_movk_i32 s4, 0x2000
	v_readfirstlane_b32 s8, v22
	v_cmp_gt_i32_e32 vcc, s4, v22
	s_and_saveexec_b64 s[4:5], vcc
	s_movk_i32 s10, 0x3c0
	s_mov_b64 s[12:13], 0x2000
	s_cbranch_execz .LBB0_1292
	s_load_dwordx2 s[6:7], s[56:57], 0xc8
	v_readlane_b32 s9, v254, 39
	v_ashrrev_i32_e32 v23, 31, v22
	v_mov_b32_e32 v5, v22
	v_lshl_add_u32 v4, v0, 6, s9
	s_waitcnt lgkmcnt(0)
	v_lshl_add_u64 v[2:3], v[22:23], 4, s[6:7]
	s_mov_b64 s[6:7], 0
	global_load_dwordx4 v[24:27], v[2:3], off
	v_lshl_add_u64 v[2:3], v[2:3], 0, s[12:13]
	global_load_dwordx4 v[28:31], v[2:3], off
	v_lshl_add_u64 v[2:3], v[2:3], 0, s[12:13]
	global_load_dwordx4 v[32:35], v[2:3], off
	v_lshl_add_u64 v[2:3], v[2:3], 0, s[12:13]
	global_load_dwordx4 v[36:39], v[2:3], off
	v_lshl_add_u64 v[2:3], v[2:3], 0, s[12:13]
	global_load_dwordx4 v[40:43], v[2:3], off
	v_lshl_add_u64 v[2:3], v[2:3], 0, s[12:13]
	global_load_dwordx4 v[44:47], v[2:3], off
	v_lshl_add_u64 v[2:3], v[2:3], 0, s[12:13]
	global_load_dwordx4 v[48:51], v[2:3], off
	v_lshl_add_u64 v[2:3], v[2:3], 0, s[12:13]
	global_load_dwordx4 v[52:55], v[2:3], off
	v_lshl_add_u64 v[2:3], v[2:3], 0, s[12:13]
	global_load_dwordx4 v[56:59], v[2:3], off
	v_lshl_add_u64 v[2:3], v[2:3], 0, s[12:13]
	global_load_dwordx4 v[60:63], v[2:3], off
	v_lshl_add_u64 v[2:3], v[2:3], 0, s[12:13]
	global_load_dwordx4 v[64:67], v[2:3], off
	v_lshl_add_u64 v[2:3], v[2:3], 0, s[12:13]
	global_load_dwordx4 v[68:71], v[2:3], off
	v_lshl_add_u64 v[2:3], v[2:3], 0, s[12:13]
	global_load_dwordx4 v[72:75], v[2:3], off
	v_lshl_add_u64 v[2:3], v[2:3], 0, s[12:13]
	global_load_dwordx4 v[76:79], v[2:3], off
	v_lshl_add_u64 v[2:3], v[2:3], 0, s[12:13]
	global_load_dwordx4 v[80:83], v[2:3], off
	v_lshl_add_u64 v[2:3], v[2:3], 0, s[12:13]
	global_load_dwordx4 v[84:87], v[2:3], off
	v_lshl_add_u64 v[2:3], v[2:3], 0, s[12:13]
	v_and_b32_e32 v10, 0xffffc00, v5
	v_and_or_b32 v10, v4, s10, v10
	v_and_b32_e32 v11, 0x3f0, v5
	v_lshlrev_b32_e32 v10, 4, v10
	v_add_u32_e32 v5, 0x200, v5
	v_add_u32_e32 v4, 0x8000, v4
	v_add3_u32 v10, 0, v11, v10
	s_waitcnt vmcnt(15)
	ds_write_b128 v10, v[24:27]
	v_and_b32_e32 v10, 0xffffc00, v5
	v_and_or_b32 v10, v4, s10, v10
	v_and_b32_e32 v11, 0x3f0, v5
	v_lshlrev_b32_e32 v10, 4, v10
	v_add_u32_e32 v5, 0x200, v5
	v_add_u32_e32 v4, 0x8000, v4
	v_add3_u32 v10, 0, v11, v10
	s_waitcnt vmcnt(14)
	ds_write_b128 v10, v[28:31]
	v_and_b32_e32 v10, 0xffffc00, v5
	v_and_or_b32 v10, v4, s10, v10
	v_and_b32_e32 v11, 0x3f0, v5
	v_lshlrev_b32_e32 v10, 4, v10
	v_add_u32_e32 v5, 0x200, v5
	v_add_u32_e32 v4, 0x8000, v4
	v_add3_u32 v10, 0, v11, v10
	s_waitcnt vmcnt(13)
	ds_write_b128 v10, v[32:35]
	v_and_b32_e32 v10, 0xffffc00, v5
	v_and_or_b32 v10, v4, s10, v10
	v_and_b32_e32 v11, 0x3f0, v5
	v_lshlrev_b32_e32 v10, 4, v10
	v_add_u32_e32 v5, 0x200, v5
	v_add_u32_e32 v4, 0x8000, v4
	v_add3_u32 v10, 0, v11, v10
	s_waitcnt vmcnt(12)
	ds_write_b128 v10, v[36:39]
	v_and_b32_e32 v10, 0xffffc00, v5
	v_and_or_b32 v10, v4, s10, v10
	v_and_b32_e32 v11, 0x3f0, v5
	v_lshlrev_b32_e32 v10, 4, v10
	v_add_u32_e32 v5, 0x200, v5
	v_add_u32_e32 v4, 0x8000, v4
	v_add3_u32 v10, 0, v11, v10
	s_waitcnt vmcnt(11)
	ds_write_b128 v10, v[40:43]
	v_and_b32_e32 v10, 0xffffc00, v5
	v_and_or_b32 v10, v4, s10, v10
	v_and_b32_e32 v11, 0x3f0, v5
	v_lshlrev_b32_e32 v10, 4, v10
	v_add_u32_e32 v5, 0x200, v5
	v_add_u32_e32 v4, 0x8000, v4
	v_add3_u32 v10, 0, v11, v10
	s_waitcnt vmcnt(10)
	ds_write_b128 v10, v[44:47]
	v_and_b32_e32 v10, 0xffffc00, v5
	v_and_or_b32 v10, v4, s10, v10
	v_and_b32_e32 v11, 0x3f0, v5
	v_lshlrev_b32_e32 v10, 4, v10
	v_add_u32_e32 v5, 0x200, v5
	v_add_u32_e32 v4, 0x8000, v4
	v_add3_u32 v10, 0, v11, v10
	s_waitcnt vmcnt(9)
	ds_write_b128 v10, v[48:51]
	v_and_b32_e32 v10, 0xffffc00, v5
	v_and_or_b32 v10, v4, s10, v10
	v_and_b32_e32 v11, 0x3f0, v5
	v_lshlrev_b32_e32 v10, 4, v10
	v_add_u32_e32 v5, 0x200, v5
	v_add_u32_e32 v4, 0x8000, v4
	v_add3_u32 v10, 0, v11, v10
	s_waitcnt vmcnt(8)
	ds_write_b128 v10, v[52:55]
	v_and_b32_e32 v10, 0xffffc00, v5
	v_and_or_b32 v10, v4, s10, v10
	v_and_b32_e32 v11, 0x3f0, v5
	v_lshlrev_b32_e32 v10, 4, v10
	v_add_u32_e32 v5, 0x200, v5
	v_add_u32_e32 v4, 0x8000, v4
	v_add3_u32 v10, 0, v11, v10
	s_waitcnt vmcnt(7)
	ds_write_b128 v10, v[56:59]
	v_and_b32_e32 v10, 0xffffc00, v5
	v_and_or_b32 v10, v4, s10, v10
	v_and_b32_e32 v11, 0x3f0, v5
	v_lshlrev_b32_e32 v10, 4, v10
	v_add_u32_e32 v5, 0x200, v5
	v_add_u32_e32 v4, 0x8000, v4
	v_add3_u32 v10, 0, v11, v10
	s_waitcnt vmcnt(6)
	ds_write_b128 v10, v[60:63]
	v_and_b32_e32 v10, 0xffffc00, v5
	v_and_or_b32 v10, v4, s10, v10
	v_and_b32_e32 v11, 0x3f0, v5
	v_lshlrev_b32_e32 v10, 4, v10
	v_add_u32_e32 v5, 0x200, v5
	v_add_u32_e32 v4, 0x8000, v4
	v_add3_u32 v10, 0, v11, v10
	s_waitcnt vmcnt(5)
	ds_write_b128 v10, v[64:67]
	v_and_b32_e32 v10, 0xffffc00, v5
	v_and_or_b32 v10, v4, s10, v10
	v_and_b32_e32 v11, 0x3f0, v5
	v_lshlrev_b32_e32 v10, 4, v10
	v_add_u32_e32 v5, 0x200, v5
	v_add_u32_e32 v4, 0x8000, v4
	v_add3_u32 v10, 0, v11, v10
	s_waitcnt vmcnt(4)
	ds_write_b128 v10, v[68:71]
	v_and_b32_e32 v10, 0xffffc00, v5
	v_and_or_b32 v10, v4, s10, v10
	v_and_b32_e32 v11, 0x3f0, v5
	v_lshlrev_b32_e32 v10, 4, v10
	v_add_u32_e32 v5, 0x200, v5
	v_add_u32_e32 v4, 0x8000, v4
	v_add3_u32 v10, 0, v11, v10
	s_waitcnt vmcnt(3)
	ds_write_b128 v10, v[72:75]
	v_and_b32_e32 v10, 0xffffc00, v5
	v_and_or_b32 v10, v4, s10, v10
	v_and_b32_e32 v11, 0x3f0, v5
	v_lshlrev_b32_e32 v10, 4, v10
	v_add_u32_e32 v5, 0x200, v5
	v_add_u32_e32 v4, 0x8000, v4
	v_add3_u32 v10, 0, v11, v10
	s_waitcnt vmcnt(2)
	ds_write_b128 v10, v[76:79]
	v_and_b32_e32 v10, 0xffffc00, v5
	v_and_or_b32 v10, v4, s10, v10
	v_and_b32_e32 v11, 0x3f0, v5
	v_lshlrev_b32_e32 v10, 4, v10
	v_add_u32_e32 v5, 0x200, v5
	v_add_u32_e32 v4, 0x8000, v4
	v_add3_u32 v10, 0, v11, v10
	s_waitcnt vmcnt(1)
	ds_write_b128 v10, v[80:83]
	v_and_b32_e32 v10, 0xffffc00, v5
	v_and_or_b32 v10, v4, s10, v10
	v_and_b32_e32 v11, 0x3f0, v5
	v_lshlrev_b32_e32 v10, 4, v10
	v_add_u32_e32 v5, 0x200, v5
	v_add_u32_e32 v4, 0x8000, v4
	v_add3_u32 v10, 0, v11, v10
	s_waitcnt vmcnt(0)
	ds_write_b128 v10, v[84:87]
